# moe1 gather GEMM: removed the compiler's loop-preheader vmcnt(0) at every unit start (the K-loop's counted waits already cover the staged tiles, as in the in-proj copy)
# speedup vs baseline: 1.0128x; 1.0128x over previous
.LBB0_2370:
	s_lshl_b32 s2, s41, 19
	s_and_b32 s50, s2, 0x180000
	s_lshl_b32 s2, s42, 8
	s_and_b32 s44, s2, 0x100
	s_cmp_lt_i32 s41, 4
	v_ashrrev_i32_e32 v187, 31, v186
	s_cselect_b64 s[2:3], -1, 0
	s_lshl_b32 s4, s44, 2
	v_lshlrev_b64 v[6:7], 21, v[186:187]
	s_add_i32 s4, s4, 0
	v_lshl_add_u64 v[6:7], s[10:11], 0, v[6:7]
	s_add_i32 s4, s4, 0x20100
	v_lshl_add_u64 v[188:189], v[6:7], 0, s[50:51]
	v_ashrrev_i32_e32 v185, 31, v184
	v_lshl_add_u32 v240, v218, 2, s4
	v_lshl_add_u32 v241, v213, 2, s4
	s_mov_b64 s[4:5], 0x100
	v_cndmask_b32_e64 v239, v4, v188, s[0:1]
	v_lshlrev_b64 v[6:7], 19, v[184:185]
	v_mov_b32_e32 v193, v3
	v_mov_b32_e32 v197, v3
	v_lshl_add_u64 v[206:207], v[4:5], 0, s[4:5]
	v_mov_b32_e32 v4, 0
	v_cndmask_b32_e64 v191, v5, v189, s[0:1]
	v_lshl_add_u64 v[200:201], s[14:15], 0, v[6:7]
	v_lshl_add_u64 v[202:203], s[18:19], 0, v[196:197]
	v_lshl_add_u64 v[204:205], s[18:19], 0, v[192:193]
	s_mov_b32 s45, -2
	s_mov_b64 s[22:23], 0
	v_mov_b32_e32 v197, v196
	v_mov_b32_e32 v193, v198
	v_mov_b32_e32 v185, v194
	v_mov_b32_e32 v187, v192
	v_mov_b64_e32 v[4:5], 0
	v_mov_b64_e32 v[6:7], 0
	v_mov_b64_e32 v[8:9], 0
	v_mov_b64_e32 v[10:11], 0
	v_mov_b64_e32 v[12:13], 0
	v_mov_b64_e32 v[14:15], 0
	v_mov_b64_e32 v[16:17], 0
	v_mov_b64_e32 v[18:19], 0
	v_mov_b64_e32 v[20:21], 0
	v_mov_b64_e32 v[22:23], 0
	v_mov_b64_e32 v[24:25], 0
	v_mov_b64_e32 v[26:27], 0
	v_mov_b64_e32 v[28:29], 0
	v_mov_b64_e32 v[30:31], 0
	v_mov_b64_e32 v[32:33], 0
	v_mov_b64_e32 v[34:35], 0
	v_mov_b64_e32 v[36:37], 0
	v_mov_b64_e32 v[38:39], 0
	v_mov_b64_e32 v[40:41], 0
	v_mov_b64_e32 v[42:43], 0
	v_mov_b64_e32 v[44:45], 0
	v_mov_b64_e32 v[46:47], 0
	v_mov_b64_e32 v[48:49], 0
	v_mov_b64_e32 v[50:51], 0
	v_mov_b64_e32 v[52:53], 0
	v_mov_b64_e32 v[54:55], 0
	v_mov_b64_e32 v[56:57], 0
	v_mov_b64_e32 v[58:59], 0
	v_mov_b64_e32 v[60:61], 0
	v_mov_b64_e32 v[62:63], 0
	v_mov_b64_e32 v[64:65], 0
	v_mov_b64_e32 v[66:67], 0
	v_mov_b64_e32 v[68:69], 0
	v_mov_b64_e32 v[70:71], 0
	v_mov_b64_e32 v[72:73], 0
	v_mov_b64_e32 v[74:75], 0
	v_mov_b64_e32 v[76:77], 0
	v_mov_b64_e32 v[78:79], 0
	v_mov_b64_e32 v[80:81], 0
	v_mov_b64_e32 v[82:83], 0
	v_mov_b64_e32 v[84:85], 0
	v_mov_b64_e32 v[86:87], 0
	v_mov_b64_e32 v[88:89], 0
	v_mov_b64_e32 v[90:91], 0
	v_mov_b64_e32 v[92:93], 0
	v_mov_b64_e32 v[94:95], 0
	v_mov_b64_e32 v[96:97], 0
	v_mov_b64_e32 v[98:99], 0
	v_mov_b64_e32 v[100:101], 0
	v_mov_b64_e32 v[102:103], 0
	v_mov_b64_e32 v[104:105], 0
	v_mov_b64_e32 v[106:107], 0
	v_mov_b64_e32 v[108:109], 0
	v_mov_b64_e32 v[110:111], 0
	v_mov_b64_e32 v[112:113], 0
	v_mov_b64_e32 v[114:115], 0
	v_mov_b64_e32 v[116:117], 0
	v_mov_b64_e32 v[118:119], 0
	v_mov_b64_e32 v[120:121], 0
	v_mov_b64_e32 v[122:123], 0
	v_mov_b64_e32 v[124:125], 0
	v_mov_b64_e32 v[126:127], 0
	v_mov_b64_e32 v[128:129], 0
	v_mov_b64_e32 v[130:131], 0
	s_branch .LBB0_2372
